# DPP (row_shr/row_bcast) wave scans and max-reduce instead of ds_bpermute round-trip chains in all three kernels
# speedup vs baseline: 1.0008x; 1.0008x over previous
.LBB0_13:
	s_or_b64 exec, exec, s[8:9]
	v_and_b32_e32 v66, 63, v0
	v_lshrrev_b32_e32 v64, 6, v0
	v_mov_b32_e32 v39, v38
	s_nop 1
	v_add_u32_dpp v39, v39, v39 row_shr:1 row_mask:0xf bank_mask:0xf bound_ctrl:0
	s_nop 1
	v_add_u32_dpp v39, v39, v39 row_shr:2 row_mask:0xf bank_mask:0xf bound_ctrl:0
	s_nop 1
	v_add_u32_dpp v39, v39, v39 row_shr:4 row_mask:0xf bank_mask:0xf bound_ctrl:0
	s_nop 1
	v_add_u32_dpp v39, v39, v39 row_shr:8 row_mask:0xf bank_mask:0xf bound_ctrl:0
	s_nop 1
	v_add_u32_dpp v39, v39, v39 row_bcast:15 row_mask:0xa bank_mask:0xf
	s_nop 1
	v_add_u32_dpp v39, v39, v39 row_bcast:31 row_mask:0xc bank_mask:0xf
	v_cmp_eq_u32_e64 s[8:9], 63, v66
	s_and_saveexec_b64 s[10:11], s[8:9]
	v_mov_b32_e32 v65, 0x18700
	v_lshl_or_b32 v65, v64, 2, v65
	ds_write_b32 v65, v39
	s_or_b64 exec, exec, s[10:11]
	v_mov_b32_e32 v65, 0x18700
	s_waitcnt lgkmcnt(0)
	s_barrier
	ds_read_b128 v[66:69], v65
	v_mov_b32_e32 v65, 0x18710
	ds_read_b128 v[70:73], v65
	v_cmp_lt_u32_e64 s[8:9], 63, v0
	s_movk_i32 s3, 0x7f
	v_sub_u32_e32 v38, v39, v38
	s_waitcnt lgkmcnt(1)
	v_cndmask_b32_e64 v65, 0, v66, s[8:9]
	v_cmp_lt_u32_e64 s[8:9], s3, v0
	s_movk_i32 s3, 0xbf
	v_mov_b32_e32 v66, 0x18720
	v_cndmask_b32_e64 v74, 0, v67, s[8:9]
	v_cmp_lt_u32_e64 s[8:9], s3, v0
	s_movk_i32 s3, 0xff
	v_add_u32_e32 v38, v65, v38
	v_cndmask_b32_e64 v75, 0, v68, s[8:9]
	v_cmp_lt_u32_e64 s[8:9], s3, v0
	s_movk_i32 s3, 0x13f
	v_add3_u32 v38, v38, v74, v75
	v_cndmask_b32_e64 v76, 0, v69, s[8:9]
	v_cmp_lt_u32_e64 s[8:9], s3, v0
	s_movk_i32 s3, 0x17f
	ds_read_b128 v[66:69], v66
	s_waitcnt lgkmcnt(1)
	v_cndmask_b32_e64 v77, 0, v70, s[8:9]
	v_cmp_lt_u32_e64 s[8:9], s3, v0
	s_movk_i32 s3, 0x1bf
	v_mov_b32_e32 v70, 0x18730
	v_cndmask_b32_e64 v78, 0, v71, s[8:9]
	v_cmp_lt_u32_e64 s[8:9], s3, v0
	s_movk_i32 s3, 0x1ff
	v_add3_u32 v38, v38, v76, v77
	v_cndmask_b32_e64 v79, 0, v72, s[8:9]
	v_cmp_lt_u32_e64 s[8:9], s3, v0
	s_movk_i32 s3, 0x23f
	ds_read_b96 v[70:72], v70
	v_cndmask_b32_e64 v73, 0, v73, s[8:9]
	v_cmp_lt_u32_e64 s[8:9], s3, v0
	s_movk_i32 s3, 0x27f
	v_add3_u32 v38, v38, v78, v79
	s_waitcnt lgkmcnt(1)
	v_cndmask_b32_e64 v66, 0, v66, s[8:9]
	v_cmp_lt_u32_e64 s[8:9], s3, v0
	s_movk_i32 s3, 0x2bf
	v_add3_u32 v38, v38, v73, v66
	v_cndmask_b32_e64 v67, 0, v67, s[8:9]
	v_cmp_lt_u32_e64 s[8:9], s3, v0
	s_movk_i32 s3, 0x2ff
	s_waitcnt lgkmcnt(0)
	v_cndmask_b32_e64 v68, 0, v68, s[8:9]
	v_cmp_lt_u32_e64 s[8:9], s3, v0
	s_movk_i32 s3, 0x33f
	v_add3_u32 v38, v38, v67, v68
	v_cndmask_b32_e64 v69, 0, v69, s[8:9]
	v_cmp_lt_u32_e64 s[8:9], s3, v0
	s_movk_i32 s3, 0x37f
	s_barrier
	v_cndmask_b32_e64 v70, 0, v70, s[8:9]
	v_cmp_lt_u32_e64 s[8:9], s3, v0
	v_add3_u32 v38, v38, v69, v70
	s_nop 0
	v_cndmask_b32_e64 v71, 0, v71, s[8:9]
	v_cmp_eq_u32_e64 s[8:9], 15, v64
	s_nop 1
	v_cndmask_b32_e64 v64, 0, v72, s[8:9]
	v_add3_u32 v38, v38, v71, v64
	v_and_b32_e32 v65, 0xffff, v38
	v_lshrrev_b32_e32 v64, 16, v38
	s_and_saveexec_b64 s[8:9], s[4:5]
	s_cbranch_execz .LBB0_17
	v_lshlrev_b32_e32 v38, 2, v0
	v_add_u32_e32 v39, 0x17700, v38
	v_add_u32_e32 v38, 0x17f00, v38
	ds_write_b32 v38, v65
	ds_write_b32 v39, v64

.LBB1_39:
	s_or_b64 exec, exec, s[0:1]
	s_waitcnt lgkmcnt(0)
	s_barrier
	v_and_b32_e32 v120, 31, v0
	v_lshlrev_b32_e32 v120, 2, v120
	global_load_dword v108, v120, s[44:45]
	global_load_dword v109, v120, s[44:45] offset:512
	global_load_dword v110, v120, s[46:47]
	global_load_dword v111, v120, s[44:45] offset:128
	global_load_dword v112, v120, s[46:47] offset:128
	global_load_dword v113, v120, s[44:45] offset:256
	global_load_dword v114, v120, s[44:45] offset:768
	global_load_dword v115, v120, s[46:47] offset:256
	global_load_dword v116, v120, s[44:45] offset:640
	global_load_dword v117, v120, s[44:45] offset:384
	global_load_dword v118, v120, s[44:45] offset:896
	global_load_dword v119, v120, s[46:47] offset:384
	ds_read_b128 v[2:5], v62
	v_mbcnt_lo_u32_b32 v6, -1, 0
	v_mbcnt_hi_u32_b32 v6, -1, v6
	v_add_u32_e32 v8, -1, v6
	v_add_u32_e32 v11, -2, v6
	s_waitcnt lgkmcnt(0)
	v_add_u32_e32 v7, v3, v2
	v_add3_u32 v5, v7, v4, v5
	v_and_b32_e32 v7, 64, v6
	v_and_b32_e32 v8, 63, v0
	v_mov_b32_e32 v11, v5
	v_cmp_gt_u32_e64 s[0:1], 32, v8
	v_lshrrev_b32_e32 v9, 6, v0
	s_nop 1
	v_add_u32_dpp v11, v11, v11 row_shr:1 row_mask:0xf bank_mask:0xf bound_ctrl:0
	s_nop 1
	v_add_u32_dpp v11, v11, v11 row_shr:2 row_mask:0xf bank_mask:0xf bound_ctrl:0
	s_nop 1
	v_add_u32_dpp v11, v11, v11 row_shr:4 row_mask:0xf bank_mask:0xf bound_ctrl:0
	s_nop 1
	v_add_u32_dpp v11, v11, v11 row_shr:8 row_mask:0xf bank_mask:0xf bound_ctrl:0
	s_nop 1
	v_add_u32_dpp v11, v11, v11 row_bcast:15 row_mask:0xa bank_mask:0xf
	s_nop 1
	v_add_u32_dpp v11, v11, v11 row_bcast:31 row_mask:0xc bank_mask:0xf
	v_cmp_eq_u32_e32 vcc, 63, v8
	s_nop 1
	s_and_saveexec_b64 s[4:5], vcc
	v_mov_b32_e32 v14, 0x16820
	v_lshl_or_b32 v14, v9, 2, v14
	ds_write_b32 v14, v11
	s_or_b64 exec, exec, s[4:5]
	v_mov_b32_e32 v14, 0x16820
	s_waitcnt lgkmcnt(0)
	s_barrier
	ds_read_b128 v[66:69], v14
	v_mov_b32_e32 v14, 0x16830
	ds_read_b128 v[70:73], v14
	v_cmp_lt_u32_e32 vcc, 63, v0
	s_movk_i32 s3, 0x7f
	s_waitcnt lgkmcnt(1)
	v_cndmask_b32_e32 v14, 0, v66, vcc
	v_cmp_lt_u32_e32 vcc, s3, v0
	s_movk_i32 s3, 0xbf
	s_nop 0
	v_cndmask_b32_e32 v16, 0, v67, vcc
	v_cmp_lt_u32_e32 vcc, s3, v0
	s_movk_i32 s3, 0xff
	s_nop 0
	v_cndmask_b32_e32 v66, 0, v68, vcc
	v_cmp_lt_u32_e32 vcc, s3, v0
	s_movk_i32 s3, 0x13f
	v_add3_u32 v14, v14, v16, v66
	v_cndmask_b32_e32 v16, 0, v69, vcc
	v_cmp_lt_u32_e32 vcc, s3, v0
	s_movk_i32 s3, 0x17f
	s_waitcnt lgkmcnt(0)
	v_cndmask_b32_e32 v66, 0, v70, vcc
	v_cmp_lt_u32_e32 vcc, s3, v0
	s_movk_i32 s3, 0x1bf
	v_add3_u32 v14, v14, v16, v66
	v_cndmask_b32_e32 v16, 0, v71, vcc
	v_cmp_lt_u32_e32 vcc, s3, v0
	s_movk_i32 s3, 0x1ff
	s_nop 0
	v_cndmask_b32_e32 v66, 0, v72, vcc
	v_cmp_lt_u32_e32 vcc, s3, v0
	v_add3_u32 v14, v14, v16, v66
	s_nop 0
	v_cndmask_b32_e32 v16, 0, v73, vcc
	v_add3_u32 v11, v14, v16, v11
	v_sub_u32_e32 v66, v11, v5
	v_add_u32_e32 v67, v66, v2
	v_add_u32_e32 v68, v67, v3
	v_mov_b32_e32 v2, 0x12810
	v_add_u32_e32 v69, v68, v4
	v_lshl_add_u32 v2, v0, 4, v2
	v_cmp_eq_u32_e32 vcc, s3, v0
	ds_write_b128 v2, v[66:69]
	ds_write_b128 v62, v[66:69]
	s_and_saveexec_b64 s[4:5], vcc
	v_mov_b32_e32 v2, 0x14810
	ds_write_b32 v2, v11
	s_or_b64 exec, exec, s[4:5]
	v_mov_b32_e32 v2, 0x14810
	s_waitcnt lgkmcnt(0)
	s_barrier
	ds_read_b32 v16, v2
	s_waitcnt lgkmcnt(0)
	v_readfirstlane_b32 s3, v16
	s_cmpk_lt_i32 s3, 0x1401
	s_cselect_b64 s[4:5], -1, 0
	s_cmpk_gt_i32 s3, 0x1400
	s_cselect_b64 s[60:61], -1, 0
	s_and_b64 vcc, exec, s[4:5]
	s_cbranch_vccnz .LBB1_49
	v_cmp_eq_u32_e32 vcc, 0, v0
	s_and_saveexec_b64 s[62:63], vcc
	s_cbranch_execz .LBB1_48
	s_mov_b64 s[66:67], exec
	v_mbcnt_lo_u32_b32 v3, s66, 0
	v_mbcnt_hi_u32_b32 v3, s67, v3
	v_add_u32_e32 v2, 0x60, v16
	v_cmp_eq_u32_e32 vcc, 0, v3
	s_and_saveexec_b64 s[64:65], vcc
	s_cbranch_execz .LBB1_47
	s_bcnt1_i32_b64 s3, s[66:67]
	v_mul_lo_u32 v4, v2, s3
	v_mov_b32_e32 v5, 0
	global_atomic_add v4, v5, v4, s[58:59] sc0

.LBB2_34:
	s_or_b64 exec, exec, s[28:29]
	s_waitcnt vmcnt(0)
	v_and_b32_e32 v0, 63, v0
	v_max_f32_e32 v1, v1, v1
	s_load_dwordx2 s[18:19], s[0:1], 0x30
	s_nop 0
	v_max_f32_dpp v1, v1, v1 row_shr:1 row_mask:0xf bank_mask:0xf bound_ctrl:0
	s_nop 1
	v_max_f32_dpp v1, v1, v1 row_shr:2 row_mask:0xf bank_mask:0xf bound_ctrl:0
	s_nop 1
	v_max_f32_dpp v1, v1, v1 row_shr:4 row_mask:0xf bank_mask:0xf bound_ctrl:0
	s_nop 1
	v_max_f32_dpp v1, v1, v1 row_shr:8 row_mask:0xf bank_mask:0xf bound_ctrl:0
	s_nop 1
	v_max_f32_dpp v1, v1, v1 row_bcast:15 row_mask:0xa bank_mask:0xf
	s_nop 1
	v_max_f32_dpp v1, v1, v1 row_bcast:31 row_mask:0xc bank_mask:0xf
	s_nop 1
	v_readlane_b32 s28, v1, 63
	s_waitcnt lgkmcnt(0)
	s_barrier
	v_cmp_eq_u32_e64 s[0:1], 0, v0
	s_and_saveexec_b64 s[20:21], s[0:1]
	s_cbranch_execz .LBB2_39
	v_mov_b32_e32 v0, 0
	v_mov_b32_e32 v1, s28
	ds_max_i32 v0, v1 offset:1568
